# XCD-affinity remap of the mLSTM phases (x1/x3/pre-pass helpers/x2 items dealt by vcu instead of blockIdx), on s11+x3early without the PROJ last-unit sc1
# speedup vs baseline: 1.0053x; 1.0048x over previous
; #define PG8_LAS __attribute__((address_space(3)))
; #define LAS __attribute__((address_space(3)))
; __global__ void __launch_bounds__(NTHREADS, 2) mega(MArgs a) {
;     extern __shared__ __attribute__((aligned(16))) unsigned char lds[];
;     PG8_LAS unsigned char* L = (PG8_LAS unsigned char*)lds;
;     unsigned char* ws = a.ws;
;     for (int u = threadIdx.x; u < (MK_LDS_BYTES - LDSCTL_OFF) / 4; u += NTHREADS) ((LAS unsigned*)(L + LDSCTL_OFF))[u] = 0u;
;     __syncthreads();
;     XcdBarrier bar = xcd_barrier_post((unsigned*)(ws + WS_CTL) + CW_BAR, (volatile LAS unsigned*)(L + MISC_OFF) + 8);
.LBB0_12:
	s_load_dwordx2 s[14:15], s[0:1], 0x68
	s_load_dwordx2 s[12:13], s[0:1], 0x60
	s_load_dwordx16 s[36:51], s[0:1], 0x0
	v_lshrrev_b32_e32 v1, 20, v0
	v_lshrrev_b32_e32 v0, 10, v0
	s_waitcnt lgkmcnt(0)
	s_add_i32 s2, s14, 1
	s_cmpk_gt_i32 s15, 0x3e8
	v_writelane_b32 v252, s2, 13
	s_cselect_b64 s[2:3], -1, 0
	s_add_u32 s6, s0, 0x70
	s_addc_u32 s7, s1, 0
	s_add_u32 s82, s12, 0x4200
	v_writelane_b32 v252, s6, 14
	s_addc_u32 s83, s13, 0
	v_or_b32_e32 v0, v0, v1
	v_writelane_b32 v252, s7, 15
	s_add_u32 s6, s12, 0x4400
	s_addc_u32 s7, s13, 0
	v_writelane_b32 v252, s6, 16
	v_and_b32_e32 v250, 63, v243
	v_mov_b32_e32 v97, 0
	v_writelane_b32 v252, s7, 17
	s_add_u32 s6, s12, 0x4500
	s_addc_u32 s7, s13, 0
	v_writelane_b32 v252, s6, 18
	v_mov_b32_e32 v242, 0x358637bd
	v_mov_b32_e32 v248, 0xff800000
	v_writelane_b32 v252, s7, 19
	s_add_u32 s6, s12, 0x4600
	s_addc_u32 s7, s13, 0
	v_writelane_b32 v252, s6, 20
	v_mov_b32_e32 v249, 0xe0000
	v_mov_b32_e32 v244, 0x41b17218
	v_writelane_b32 v252, s7, 21
	s_add_u32 s6, s12, 0x4700
	s_addc_u32 s7, s13, 0
	v_writelane_b32 v252, s6, 22
	s_movk_i32 s27, 0x2000
	s_movk_i32 s91, 0x3800
	v_writelane_b32 v252, s7, 23
	s_add_u32 s6, s12, 0x4800
	s_addc_u32 s7, s13, 0
	v_writelane_b32 v252, s6, 24
	s_mov_b32 s96, 0x38000
	s_mov_b32 s97, 0x3fffffc
	v_writelane_b32 v252, s7, 25
	s_add_u32 s6, s12, 0x4900
	s_addc_u32 s7, s13, 0
	v_writelane_b32 v252, s6, 26
	s_mov_b32 s29, 0
	s_mov_b64 s[30:31], 0xe0000
	v_writelane_b32 v252, s7, 27
	s_add_u32 s6, s12, 0x4a00
	s_addc_u32 s7, s13, 0
	v_writelane_b32 v252, s6, 28
	s_mov_b64 s[62:63], 0x80
	s_nop 0
	v_writelane_b32 v252, s7, 29
	s_add_u32 s6, s12, 0x4b00
	s_addc_u32 s7, s13, 0
	v_writelane_b32 v252, s6, 30
	s_nop 1
	v_writelane_b32 v252, s7, 31
	s_add_u32 s6, s12, 0x4c00
	s_addc_u32 s7, s13, 0
	v_writelane_b32 v252, s6, 32
	s_nop 1
	v_writelane_b32 v252, s7, 33
	s_add_u32 s6, s12, 0x4d00
	s_addc_u32 s7, s13, 0
	v_writelane_b32 v252, s6, 34
	s_nop 1
	v_writelane_b32 v252, s7, 35
	s_add_u32 s6, s12, 0x4e00
	s_addc_u32 s7, s13, 0
	v_writelane_b32 v252, s6, 36
	s_nop 1
	v_writelane_b32 v252, s7, 37
	s_add_u32 s6, s12, 0x4f00
	s_addc_u32 s7, s13, 0
	v_writelane_b32 v252, s6, 38
	s_nop 1
	v_writelane_b32 v252, s7, 39
	s_add_u32 s6, s12, 0x5000
	s_addc_u32 s7, s13, 0
	v_writelane_b32 v252, s6, 40
	s_nop 1
	v_writelane_b32 v252, s7, 41
	s_add_u32 s6, s12, 0x5100
	s_addc_u32 s7, s13, 0
	v_writelane_b32 v252, s6, 42
	s_nop 1
	v_writelane_b32 v252, s7, 43
	s_add_u32 s6, s12, 0x5200
	s_addc_u32 s7, s13, 0
	v_writelane_b32 v252, s6, 44
	s_nop 1
	v_writelane_b32 v252, s7, 45
	s_add_u32 s6, s12, 0x5300
	s_addc_u32 s7, s13, 0
	v_writelane_b32 v252, s6, 46
	s_cmp_eq_u32 s8, 15
	s_nop 0
	v_writelane_b32 v252, s7, 47
	s_cselect_b64 s[6:7], -1, 0
	v_writelane_b32 v252, s6, 48
	s_cmp_eq_u32 s8, 14
	s_nop 0
	v_writelane_b32 v252, s7, 49
	s_cselect_b64 s[6:7], -1, 0
	v_writelane_b32 v252, s6, 50
	s_cmp_eq_u32 s8, 13
	s_nop 0
	v_writelane_b32 v252, s7, 51
	s_cselect_b64 s[6:7], -1, 0
	v_writelane_b32 v252, s6, 52
	s_cmp_eq_u32 s8, 12
	s_nop 0
	v_writelane_b32 v252, s7, 53
	s_cselect_b64 s[6:7], -1, 0
	v_writelane_b32 v252, s6, 54
	s_cmp_eq_u32 s8, 11
	s_nop 0
	v_writelane_b32 v252, s7, 55
	s_cselect_b64 s[6:7], -1, 0
	v_writelane_b32 v252, s6, 56
	s_cmp_eq_u32 s8, 10
	s_nop 0
	v_writelane_b32 v252, s7, 57
	s_cselect_b64 s[6:7], -1, 0
	v_writelane_b32 v252, s6, 58
	s_cmp_eq_u32 s8, 9
	s_nop 0
	v_writelane_b32 v252, s7, 59
	s_cselect_b64 s[6:7], -1, 0
	v_writelane_b32 v252, s6, 60
	s_cmp_eq_u32 s8, 8
	s_nop 0
	v_writelane_b32 v252, s7, 61
	s_cselect_b64 s[6:7], -1, 0
	v_writelane_b32 v252, s6, 62
	s_cmp_eq_u32 s8, 7
	s_nop 0
	v_writelane_b32 v252, s7, 63
	s_cselect_b64 s[6:7], -1, 0
	v_writelane_b32 v253, s6, 0
	s_cmp_eq_u32 s8, 6
	v_readlane_b32 s11, v252, 0
	v_writelane_b32 v253, s7, 1
	s_cselect_b64 s[6:7], -1, 0
	v_writelane_b32 v253, s6, 2
	s_cmp_eq_u32 s8, 5
	v_readlane_b32 s16, v252, 3
	v_writelane_b32 v253, s7, 3
	s_cselect_b64 s[6:7], -1, 0
	v_writelane_b32 v253, s6, 4
	s_cmp_eq_u32 s8, 4
	v_readlane_b32 s22, v252, 9
	v_writelane_b32 v253, s7, 5
	s_cselect_b64 s[6:7], -1, 0
	v_writelane_b32 v253, s6, 6
	s_cmp_eq_u32 s8, 3
	v_readlane_b32 s23, v252, 10
	v_writelane_b32 v253, s7, 7
	s_cselect_b64 s[6:7], -1, 0
	v_writelane_b32 v253, s6, 8
	s_cmp_eq_u32 s8, 2
	v_readlane_b32 s17, v252, 4
	v_writelane_b32 v253, s7, 9
	s_cselect_b64 s[6:7], -1, 0
	v_writelane_b32 v253, s6, 10
	s_cmp_eq_u32 s8, 1
	v_readlane_b32 s18, v252, 5
	v_writelane_b32 v253, s7, 11
	s_cselect_b64 s[6:7], -1, 0
	v_writelane_b32 v253, s6, 12
	s_cmp_eq_u32 s8, 0
	v_readlane_b32 s19, v252, 6
	v_writelane_b32 v253, s7, 13
	s_cselect_b64 s[6:7], -1, 0
	v_writelane_b32 v253, s6, 14
	v_readlane_b32 s20, v252, 7
	v_readlane_b32 s21, v252, 8
	v_writelane_b32 v253, s7, 15
	s_lshl_b32 s6, s8, 8
	s_add_u32 s4, s4, s6
	s_addc_u32 s5, s5, 0
	s_add_u32 s6, s4, 0x1400
	s_addc_u32 s7, s5, 0
	v_writelane_b32 v253, s6, 16
	s_nop 1
	v_writelane_b32 v253, s7, 17
	s_add_u32 s6, s4, 0x2400
	s_addc_u32 s7, s5, 0
	v_writelane_b32 v253, s6, 18
	s_nop 1
	v_writelane_b32 v253, s7, 19
	s_add_u32 s6, s12, 0x7400
	s_addc_u32 s7, s13, 0
	v_writelane_b32 v253, s6, 20
	s_nop 1
	v_writelane_b32 v253, s7, 21
	s_add_u32 s6, s12, 0x7500
	s_addc_u32 s7, s13, 0
	v_writelane_b32 v253, s6, 22
	s_nop 1
	v_writelane_b32 v253, s7, 23
	s_add_u32 s6, s12, 0x3400000
	s_addc_u32 s7, s13, 0
	v_writelane_b32 v253, s6, 24
	s_nop 1
	v_writelane_b32 v253, s7, 25
	s_mul_i32 s6, s11, 5
	s_add_i32 s6, s6, -3
	s_add_u32 s84, s12, 0x9000
	s_addc_u32 s85, s13, 0
	s_add_u32 s24, s12, 0x1c400000
	s_addc_u32 s25, s13, 0
	v_writelane_b32 v253, s6, 26
	s_add_u32 s6, s12, 0xc00000
; #define PG8_LAS __attribute__((address_space(3)))
; #define LAS __attribute__((address_space(3)))
; __global__ void __launch_bounds__(NTHREADS, 2) mega(MArgs a) {
;     extern __shared__ __attribute__((aligned(16))) unsigned char lds[];
;     PG8_LAS unsigned char* L = (PG8_LAS unsigned char*)lds;
;     unsigned char* ws = a.ws;
;     for (int u = threadIdx.x; u < (MK_LDS_BYTES - LDSCTL_OFF) / 4; u += NTHREADS) ((LAS unsigned*)(L + LDSCTL_OFF))[u] = 0u;
;     __syncthreads();
;     XcdBarrier bar = xcd_barrier_post((unsigned*)(ws + WS_CTL) + CW_BAR, (volatile LAS unsigned*)(L + MISC_OFF) + 8);
;     ...
;             const int vcu = (G % 8 == 0) ? (bx % 8) * (G / 8) + bx / 8 : bx;
	s_addc_u32 s7, s13, 0
	v_writelane_b32 v253, s6, 27
	s_nop 1
	v_writelane_b32 v253, s7, 28
	s_add_u32 s6, s12, 0xa0000
	s_addc_u32 s7, s13, 0
	v_writelane_b32 v253, s6, 29
	s_nop 1
	v_writelane_b32 v253, s7, 30
	s_add_u32 s6, s12, 0x10000
	v_writelane_b32 v253, s6, 31
	s_addc_u32 s6, s13, 0
	s_cmpk_lt_i32 s11, 0x100
	v_writelane_b32 v253, s6, 32
	s_cselect_b64 s[6:7], -1, 0
	v_writelane_b32 v253, s6, 33
	s_nop 1
	v_writelane_b32 v253, s7, 34
	s_ashr_i32 s6, s11, 31
	v_writelane_b32 v253, s6, 35
	s_lshr_b32 s6, s6, 29
	s_add_i32 s6, s11, s6
	s_ashr_i32 s15, s6, 3
	s_and_b32 s6, s6, -8
	s_sub_i32 s26, s11, s6
	s_lshl_b32 s6, s26, 5
	s_add_u32 s0, s38, 0x1000
	v_writelane_b32 v253, s36, 36
	s_addc_u32 s1, s39, 0
	s_nop 0
	v_writelane_b32 v253, s37, 37
	v_writelane_b32 v253, s38, 38
	v_writelane_b32 v253, s39, 39
	v_writelane_b32 v253, s40, 40
	v_writelane_b32 v253, s41, 41
	v_writelane_b32 v253, s42, 42
	v_writelane_b32 v253, s43, 43
	v_writelane_b32 v253, s44, 44
	v_writelane_b32 v253, s45, 45
	v_writelane_b32 v253, s46, 46
	v_writelane_b32 v253, s47, 47
	v_writelane_b32 v253, s48, 48
	v_writelane_b32 v253, s49, 49
	v_writelane_b32 v253, s50, 50
	v_writelane_b32 v253, s51, 51
	v_writelane_b32 v253, s0, 52
	s_mov_b32 s44, 0x800000
	s_mov_b32 s48, 0xe0000
	v_writelane_b32 v253, s1, 53
	s_add_u32 s0, s22, 0x4000000
	s_addc_u32 s1, s23, 0
	v_writelane_b32 v253, s0, 54
	s_mov_b32 s22, 0xfff20000
	s_mov_b32 s49, 0x41400000
	v_writelane_b32 v253, s1, 55
	s_add_u32 s0, s12, 0x1a400000
	v_writelane_b32 v253, s0, 56
	s_addc_u32 s0, s13, 0
	v_writelane_b32 v253, s0, 57
	s_add_u32 s0, s12, 0x5400000
	v_writelane_b32 v253, s0, 58
	s_addc_u32 s0, s13, 0
	v_writelane_b32 v253, s0, 59
	s_add_u32 s0, s12, 0x600000
	s_addc_u32 s1, s13, 0
	v_writelane_b32 v253, s0, 60
	s_mov_b32 s45, s14
	s_mov_b32 s23, -1
	v_writelane_b32 v253, s1, 61
	s_add_u32 s0, s12, 0xc403000
	s_addc_u32 s1, s13, 0
	v_writelane_b32 v253, s0, 62
	s_nop 1
	v_writelane_b32 v253, s1, 63
	s_add_u32 s0, s4, 0x4000
	s_addc_u32 s1, s5, 0
	v_writelane_b32 v254, s0, 0
	s_nop 1
	v_writelane_b32 v254, s1, 1
	s_add_u32 s0, s12, 0xe0000
	s_addc_u32 s1, s13, 0
	s_add_u32 s86, s12, 0x100000
	s_addc_u32 s87, s13, 0
	v_writelane_b32 v254, s0, 2
	s_cmpk_gt_i32 s11, 0xff
	s_nop 0
	v_writelane_b32 v254, s1, 3
	s_cselect_b64 s[0:1], -1, 0
	s_add_u32 s4, s12, 0x1000000
	s_addc_u32 s5, s13, 0
	s_add_u32 s16, s12, 0xc400000
	s_addc_u32 s17, s13, 0
	v_writelane_b32 v254, s4, 4
	s_cmpk_lt_i32 s11, 0x600
	s_nop 0
	v_writelane_b32 v254, s5, 5
	s_cselect_b64 s[4:5], -1, 0
	v_writelane_b32 v254, s4, 6
	s_nop 1
	v_writelane_b32 v254, s5, 7
	s_lshl_b32 s4, s11, 2
	s_add_u32 s88, s12, 0xb400000
	s_addc_u32 s89, s13, 0
	s_add_u32 s79, s12, 0xa400000
	s_addc_u32 s90, s13, 0
	s_add_u32 s92, s12, 0x580000
	s_addc_u32 s93, s13, 0
	s_add_u32 s94, s12, 0x484000
	s_addc_u32 s95, s13, 0
	s_add_u32 s5, s12, 0x300000
	v_writelane_b32 v254, s5, 8
	s_addc_u32 s5, s13, 0
	v_writelane_b32 v254, s5, 9
	s_add_u32 s5, s12, 0x400000
	v_writelane_b32 v254, s5, 10
	s_addc_u32 s5, s13, 0
	v_writelane_b32 v254, s5, 11
	s_add_u32 s5, s12, 0xc401000
	v_writelane_b32 v254, s5, 12
	s_addc_u32 s5, s13, 0
	v_writelane_b32 v254, s5, 13
	s_add_u32 s5, s12, 0xc401400
	v_writelane_b32 v254, s5, 14
	s_addc_u32 s5, s13, 0
	v_writelane_b32 v254, s5, 15
	s_add_u32 s5, s12, 0xc401800
	v_writelane_b32 v254, s5, 16
	s_addc_u32 s5, s13, 0
	v_writelane_b32 v254, s5, 17
	s_add_u32 s5, s12, 0xc401c00
	v_writelane_b32 v254, s5, 18
	s_addc_u32 s5, s13, 0
	v_writelane_b32 v254, s5, 19
	s_add_u32 s5, s12, 0x5400400
	v_writelane_b32 v254, s5, 20
	s_addc_u32 s5, s13, 0
	v_writelane_b32 v254, s5, 21
	s_add_u32 s5, s12, 0xc400400
	v_writelane_b32 v254, s5, 22
	s_addc_u32 s5, s13, 0
	v_writelane_b32 v254, s5, 23
	s_add_u32 s5, s12, 0xc400800
	v_writelane_b32 v254, s5, 24
	s_addc_u32 s5, s13, 0
	v_writelane_b32 v254, s5, 25
	s_add_u32 s5, s12, 0xc400c00
	v_writelane_b32 v254, s5, 26
	s_addc_u32 s5, s13, 0
	v_writelane_b32 v254, s5, 27
	s_add_u32 s5, s12, 0x8400000
	v_writelane_b32 v254, s5, 28
	s_addc_u32 s5, s13, 0
	s_add_u32 s8, s12, 0x500000
	v_writelane_b32 v254, s5, 29
	s_addc_u32 s9, s13, 0
	v_writelane_b32 v254, s8, 30
	s_nop 1
	v_writelane_b32 v254, s9, 31
	s_add_u32 s8, s12, 0x482000
	s_addc_u32 s9, s13, 0
	v_writelane_b32 v254, s8, 32
	s_nop 1
	v_writelane_b32 v254, s9, 33
	s_add_u32 s8, s12, 0x480000
	s_addc_u32 s9, s13, 0
	v_writelane_b32 v254, s8, 34
	s_nop 1
	v_writelane_b32 v254, s9, 35
	s_and_b32 s4, s11, 7
; __global__ void __launch_bounds__(NTHREADS, 2) mega(MArgs a) {
;     ...
;             const int vcu = (G % 8 == 0) ? (bx % 8) * (G / 8) + bx / 8 : bx;
	s_lshl_b32 s4, s4, 5
	s_lshr_b32 s100, s11, 3
	s_add_i32 s4, s4, s100
	s_lshl_b32 s4, s4, 2
	v_writelane_b32 v254, s4, 36
	s_add_i32 s4, s4, -4
	v_writelane_b32 v254, s4, 37
	s_lshl_b32 s4, s11, 3
	v_writelane_b32 v254, s4, 38
	s_add_u32 s4, s12, 0x80000
	s_addc_u32 s5, s13, 0
	v_writelane_b32 v254, s4, 39
	s_cmp_lt_i32 s26, 0
	s_nop 0
	v_writelane_b32 v254, s5, 40
	s_mul_i32 s4, s26, 33
	s_cselect_b32 s4, s4, s6
	s_movk_i32 s5, 0xc1
	s_cselect_b32 s6, s5, 0xc0
	s_add_i32 s7, s4, s15
	s_ashr_i32 s8, s7, 31
	s_lshr_b32 s4, s8, 29
	s_add_i32 s4, s7, s4
	s_and_b32 s5, s4, 0xfff8
	s_sub_i32 s5, s7, s5
	s_bfe_u32 s9, s5, 0x10007
	s_add_i32 s9, s5, s9
	s_and_b32 s10, s9, 0xfe
	s_sub_i32 s5, s5, s10
	s_ashr_i32 s4, s4, 3
	s_bfe_i32 s9, s9, 0x80000
	s_lshl_b32 s4, s4, 1
	s_sext_i32_i16 s9, s9
	s_sext_i32_i8 s5, s5
	s_add_i32 s12, s4, s5
	s_ashr_i32 s4, s9, 1
	v_writelane_b32 v254, s4, 41
	s_lshr_b32 s4, s9, 1
	s_bfe_i64 s[4:5], s[4:5], 0x100000
	s_lshl_b64 s[4:5], s[4:5], 19
	v_writelane_b32 v254, s4, 42
	s_ashr_i32 s13, s12, 31
	s_mul_i32 s6, s26, s6
	v_writelane_b32 v254, s5, 43
	s_mov_b32 s4, s12
	v_writelane_b32 v254, s4, 44
	s_nop 1
	v_writelane_b32 v254, s5, 45
	s_lshl_b64 s[4:5], s[12:13], 19
	s_add_u32 s12, s24, s4
	v_writelane_b32 v254, s24, 46
	s_addc_u32 s13, s25, s5
	s_movk_i32 s4, 0x3ff
	v_writelane_b32 v254, s25, 47
	v_and_or_b32 v0, v0, s4, v243
	s_add_u32 s4, s12, 0x40000
	v_writelane_b32 v254, s12, 48
	s_addc_u32 s5, s13, 0
	s_add_i32 s6, s6, s15
	v_writelane_b32 v254, s13, 49
	v_writelane_b32 v254, s4, 50
	s_xor_b64 s[2:3], s[2:3], -1
	s_xor_b64 s[0:1], s[0:1], -1
	v_writelane_b32 v254, s5, 51
	s_lshr_b32 s4, s8, 27
	s_add_i32 s4, s7, s4
	s_and_b32 s5, s4, 0xffe0
	s_sub_i32 s5, s7, s5
	s_bfe_i32 s7, s5, 0x80000
	s_bfe_u32 s7, s7, 0x3000c
	s_add_i32 s7, s5, s7
	s_and_b32 s8, s7, 0xf8
	s_sub_i32 s5, s5, s8
	s_mul_hi_i32 s8, s6, 0x2aaaaaab
	s_lshr_b32 s9, s8, 31
	s_ashr_i32 s8, s8, 4
	s_add_i32 s8, s8, s9
	s_mul_i32 s9, s8, 0x60
	s_sub_i32 s6, s6, s9
	s_bfe_i32 s9, s6, 0x80000
	s_bfe_u32 s9, s9, 0x2000d
	s_add_i32 s9, s6, s9
	s_ashr_i32 s4, s4, 5
	s_and_b32 s10, s9, 0xfc
	s_lshl_b32 s4, s4, 3
	s_sext_i32_i8 s5, s5
	s_sub_i32 s6, s6, s10
	s_add_i32 s12, s4, s5
	s_bfe_i32 s5, s9, 0x80000
	v_writelane_b32 v254, s26, 52
	s_lshl_b32 s4, s8, 2
	s_sext_i32_i16 s5, s5
	s_sext_i32_i8 s6, s6
	v_writelane_b32 v254, s15, 53
	s_add_i32 s8, s4, s6
	s_ashr_i32 s4, s5, 2
	v_writelane_b32 v254, s4, 54
	s_lshr_b32 s4, s5, 2
	s_bfe_i64 s[4:5], s[4:5], 0x100000
	s_bfe_i32 s7, s7, 0x80000
	s_lshl_b64 s[4:5], s[4:5], 19
	s_sext_i32_i16 s7, s7
	v_writelane_b32 v254, s4, 55
	s_ashr_i32 s9, s8, 31
	s_ashr_i32 s13, s12, 31
	v_writelane_b32 v254, s5, 56
	s_ashr_i32 s4, s7, 3
	v_writelane_b32 v254, s4, 57
	s_lshr_b32 s4, s7, 3
	s_bfe_i64 s[4:5], s[4:5], 0x100000
	s_lshl_b64 s[4:5], s[4:5], 19
	v_writelane_b32 v254, s4, 58
	s_mov_b32 s24, 0xffe40000
	s_movk_i32 s7, 0xc00
	v_writelane_b32 v254, s5, 59
	s_mul_i32 s4, s11, 10
	s_add_i32 s4, s4, -5
	v_writelane_b32 v254, s4, 60
	v_writelane_b32 v254, s2, 61
	s_add_i32 s33, 0, 0x14800
	s_mov_b32 s25, -1
	v_writelane_b32 v254, s3, 62
	v_writelane_b32 v254, s0, 63
	s_nop 1
	v_writelane_b32 v255, s1, 0
	s_lshl_b32 s0, s11, 4
	v_writelane_b32 v255, s0, 1
	s_add_i32 s0, 0, 0x20160
	v_writelane_b32 v255, s0, 2
	s_add_i32 s0, 0, 0x20164
	v_writelane_b32 v255, s0, 3
	s_add_i32 s0, 0, 0x15000
	v_writelane_b32 v255, s0, 4
	v_cmp_eq_u32_e64 s[0:1], 0, v0
	s_nop 1
	v_writelane_b32 v255, s0, 5
	s_nop 1
	v_writelane_b32 v255, s1, 6
	s_mov_b32 s0, s8
	v_writelane_b32 v255, s0, 7
	s_nop 1
	v_writelane_b32 v255, s1, 8
	s_lshl_b64 s[0:1], s[8:9], 19
	v_writelane_b32 v255, s0, 9
	s_mov_b64 s[8:9], 0x1c0000
	s_nop 0
	v_writelane_b32 v255, s1, 10
	s_mov_b32 s0, s12
	v_writelane_b32 v255, s0, 11
	s_nop 1
	v_writelane_b32 v255, s1, 12
	s_lshl_b64 s[0:1], s[12:13], 19
	v_writelane_b32 v255, s0, 13
	s_nop 1
	v_writelane_b32 v255, s1, 14
	v_writelane_b32 v255, s80, 15
	s_nop 1
	v_writelane_b32 v255, s81, 16
	v_writelane_b32 v255, s82, 17
	s_nop 1
	v_writelane_b32 v255, s83, 18
	v_writelane_b32 v255, s84, 19
	s_nop 1
	v_writelane_b32 v255, s85, 20
	v_writelane_b32 v255, s86, 21
	s_nop 1
	v_writelane_b32 v255, s87, 22
	v_writelane_b32 v255, s88, 23
	s_nop 1
	v_writelane_b32 v255, s89, 24
	v_writelane_b32 v255, s79, 25
	v_writelane_b32 v255, s90, 26
	v_writelane_b32 v255, s92, 27
	v_writelane_b32 v255, s93, 28
	v_writelane_b32 v255, s94, 29
	v_writelane_b32 v255, s95, 30
	s_branch .LBB0_16

; __global__ void __launch_bounds__(NTHREADS, 2) mega(MArgs a) {
;     ...
;         } else if (ph == PH_SCAN) {
;             xcd_split_wait(bar, ub + 1u);
;             for (int it = blockIdx.x; it < 32 * 8; it += gridDim.x)
;                 mlstm::x2_item(it, hf * HB, (const h16*)(ws + WS_U), (const float*)(ws + WS_MUN), (const float*)(ws + WS_MAMAX), (const float*)(ws + WS_MBLAST),
;                                (h16*)(ws + WS_CS), (float*)(ws + WS_MNS), (float*)(ws + WS_MMS), (char*)lds);
.LBB0_753:
	s_or_b64 exec, exec, s[0:1]
	v_readlane_b32 s0, v253, 33
	v_readlane_b32 s1, v253, 34
	s_andn2_b64 vcc, exec, s[0:1]
	s_waitcnt vmcnt(0) lgkmcnt(0)
	s_barrier
	s_cbranch_vccnz .LBB0_854
	v_readlane_b32 s0, v255, 42
	s_lshl_b32 s4, s0, 5
	v_readlane_b32 s5, v254, 36
	s_lshr_b32 s5, s5, 2
	s_branch .LBB0_756
